# S1 static work split rebalanced: a heavy context item counts as 8 light slots (was 7), since light items sped up more than the heavy one
# speedup vs baseline: 1.0056x; 1.0056x over previous
.LBB0_436:
	s_mov_b32 s33, 8
	s_movk_i32 s0, 0xff80
	s_mov_b32 s1, s73
	v_readlane_b32 s21, v241, 41
	v_readlane_b32 s2, v241, 49
	s_branch .LBB0_468

.LBB0_470:
	s_add_i32 s21, s33, 1
	s_cmp_lt_u32 s33, 7
	v_readlane_b32 s20, v243, 63
	s_cselect_b32 s20, s20, s73
	s_cselect_b32 s27, -16, 0xffffff80
	s_add_i32 s27, s27, s74
	s_mul_i32 s20, s20, s21
	s_add_i32 s20, s27, s20
	s_cmpk_lt_i32 s20, 0x7e0
	s_mov_b32 s33, s21
	s_cbranch_scc0 .LBB0_496
